# mixer-B: all eight K fragments pre-read at the end of the softmax section (was four); LDS writes grouped late
# baseline (speedup 1.0000x reference)
; #define ATT_SBAR() __builtin_amdgcn_sched_barrier(0)
; #define ATT_PK4(P, BASE, OUT) do { u32x4 w = {cvtpk(P[BASE + 0], P[BASE + 1]), cvtpk(P[BASE + 2], P[BASE + 3]), cvtpk(P[BASE + 4], P[BASE + 5]), cvtpk(P[BASE + 6], P[BASE + 7])}; \
;     OUT = *reinterpret_cast<bf16x8*>(&w); } while (0)
; #define ATT_WRITE_K(so) do { *(bf16x8*)(K_lds + (so) + kswz<DQK>(kr, kc * 2)) = sk0; if constexpr (DQK == 128) *(bf16x8*)(K_lds + (so) + kswz<DQK>(32 + kr, kc * 2)) = sk1; } while (0)
; #define ATT_WRITE_V(so) do { *(bf16x8*)(V_lds + (so) + vst0) = sv0; *(bf16x8*)(V_lds + (so) + vst1) = sv1; } while (0)
; #define ATT_BAR() do { ATT_SBAR(); asm volatile("s_barrier" ::: "memory"); ATT_SBAR(); } while (0)
; #define ATT_VPAIR(buf, so, blk, ks) do { if constexpr (!(ABL & 8) && !(ABL & 32)) { buf[2 * (ks)] = vtr(vq0 + (so) + v_rd_off(blk, ks, 0)); buf[2 * (ks) + 1] = vtr(vq0 + (so) + v_rd_off(blk, ks, 1)); } } while (0)
; __device__ __forceinline__ void softmax_exp_pack(f32x16& p0, f32x16& p1, bf16x8& pa0, bf16x8& pa1, bf16x8& pa2, bf16x8& pa3) {
; #pragma unroll
;   for (int r = 0; r < 16; ++r) { p0[r] = __builtin_amdgcn_exp2f(p0[r]); p1[r] = __builtin_amdgcn_exp2f(p1[r]); }
;     ...
;   ATT_PK4(p0, 0, pa0); ATT_PK4(p0, 8, pa1); ATT_PK4(p1, 0, pa2); ATT_PK4(p1, 8, pa3);
;     ...
;     if constexpr (!(ABL & 4)) { ATT_WRITE_K(k2); ATT_WRITE_V(v1); }
;     ATT_SBAR();
; #pragma unroll
;     for (int ks = 0; ks < 4; ++ks) ATT_VPAIR(va, v0, 0, ks);
;     asm volatile("s_waitcnt lgkmcnt(8)" ::: "memory"); ATT_BAR();
.LBB0_283:
	v_exp_f32_e32 v98, v98
	v_exp_f32_e32 v114, v114
	v_exp_f32_e32 v99, v99
	v_exp_f32_e32 v115, v115
	v_exp_f32_e32 v100, v100
	v_exp_f32_e32 v101, v101
	v_exp_f32_e32 v102, v102
	v_exp_f32_e32 v103, v103
	v_exp_f32_e32 v106, v106
	v_exp_f32_e32 v107, v107
	v_exp_f32_e32 v116, v116
	v_exp_f32_e32 v117, v117
	v_exp_f32_e32 v118, v118
	v_exp_f32_e32 v119, v119
	v_exp_f32_e32 v104, v104
	v_exp_f32_e32 v120, v120
	v_exp_f32_e32 v105, v105
	v_exp_f32_e32 v121, v121
	v_exp_f32_e32 v122, v122
	v_exp_f32_e32 v123, v123
	v_exp_f32_e32 v108, v108
	v_exp_f32_e32 v124, v124
	v_exp_f32_e32 v109, v109
	v_exp_f32_e32 v125, v125
	v_exp_f32_e32 v110, v110
	v_exp_f32_e32 v126, v126
	v_exp_f32_e32 v111, v111
	v_exp_f32_e32 v127, v127
	v_exp_f32_e32 v112, v112
	v_exp_f32_e32 v128, v128
	v_exp_f32_e32 v113, v113
	v_exp_f32_e32 v129, v129
	v_cvt_pk_bf16_f32 v2, v98, v99
	v_cvt_pk_bf16_f32 v3, v100, v101
	v_cvt_pk_bf16_f32 v4, v102, v103
	v_cvt_pk_bf16_f32 v6, v106, v107
	v_cvt_pk_bf16_f32 v10, v114, v115
	v_cvt_pk_bf16_f32 v5, v104, v105
	v_cvt_pk_bf16_f32 v7, v108, v109
	v_cvt_pk_bf16_f32 v8, v110, v111
	v_cvt_pk_bf16_f32 v9, v112, v113
	v_cvt_pk_bf16_f32 v11, v116, v117
	v_cvt_pk_bf16_f32 v12, v118, v119
	v_cvt_pk_bf16_f32 v13, v120, v121
	v_cvt_pk_bf16_f32 v14, v122, v123
	v_cvt_pk_bf16_f32 v15, v124, v125
	v_cvt_pk_bf16_f32 v16, v126, v127
	v_cvt_pk_bf16_f32 v17, v128, v129
	s_waitcnt vmcnt(0)
	v_add_u32_e32 v114, s94, v169
	ds_write_b128 v114, v[224:227] offset:49152
	v_add_u32_e32 v114, s95, v167
	ds_write_b128 v114, v[228:231]
	v_add_u32_e32 v114, s95, v168
	ds_write_b128 v114, v[232:235]
	v_add_u32_e32 v249, s96, v172
	ds_read_b128 v[152:155], v249 offset:49152
	ds_read_b128 v[156:159], v249 offset:53760
	ds_read_b128 v[160:163], v249 offset:49184
	ds_read_b128 v[176:179], v249 offset:53792
	ds_read_b128 v[180:183], v249 offset:49216
	ds_read_b128 v[186:189], v249 offset:53824
	ds_read_b128 v[190:193], v249 offset:49248
	ds_read_b128 v[194:197], v249 offset:53856
	s_waitcnt lgkmcnt(8)
	s_barrier
; #define ATT_SBAR() __builtin_amdgcn_sched_barrier(0)
; __device__ __forceinline__ float softmax_rowmax(const f32x16& p0, const f32x16& p1) {
;   const float m0 = p1[0] + 0.0f; float a, b;
;   asm("v_max3_f32 %0, %1, %2, %3\n\tv_max3_f32 %0, %0, %4, %5\n\tv_max3_f32 %0, %0, %6, %7\n\tv_max3_f32 %0, %0, %8, %9\n\t"
;       "v_max3_f32 %0, %0, %10, %11\n\tv_max3_f32 %0, %0, %12, %13\n\tv_max3_f32 %0, %0, %14, %15\n\tv_max3_f32 %0, %0, %16, %17"
;       : "=&v"(a) : "v"(m0), "v"(p0[0]), "v"(p0[1]), "v"(p0[2]), "v"(p0[3]), "v"(p0[4]), "v"(p0[5]), "v"(p0[6]), "v"(p0[7]), "v"(p0[8]), "v"(p0[9]), "v"(p0[10]), "v"(p0[11]), "v"(p0[12]), "v"(p0[13]), "v"(p0[14]), "v"(p0[15]));
;   asm("v_max3_f32 %0, %1, %2, %3\n\tv_max3_f32 %0, %0, %4, %5\n\tv_max3_f32 %0, %0, %6, %7\n\tv_max3_f32 %0, %0, %8, %9\n\t"
;       "v_max3_f32 %0, %0, %10, %11\n\tv_max3_f32 %0, %0, %12, %13\n\tv_max3_f32 %0, %0, %14, %15\n\tv_max_f32 %0, %0, %16"
;       : "=&v"(b) : "v"(a), "v"(p1[1]), "v"(p1[2]), "v"(p1[3]), "v"(p1[4]), "v"(p1[5]), "v"(p1[6]), "v"(p1[7]), "v"(p1[8]), "v"(p1[9]), "v"(p1[10]), "v"(p1[11]), "v"(p1[12]), "v"(p1[13]), "v"(p1[14]), "v"(p1[15]));
;   return b;
;     ...
;   for (int t = 0; t + 1 < NT; ++t) {
;     if constexpr (ABL & 1) { u32x4 w0 = {cvtpk(p0[0], p0[1]), cvtpk(p0[2], p0[3]), cvtpk(p0[4], p0[5]), cvtpk(p0[6], p0[7])}, w1 = {cvtpk(p0[8], p0[9]), cvtpk(p0[10], p0[11]), cvtpk(p0[12], p0[13]), cvtpk(p0[14], p0[15])};
;         u32x4 w2 = {cvtpk(p1[0], p1[1]), cvtpk(p1[2], p1[3]), cvtpk(p1[4], p1[5]), cvtpk(p1[6], p1[7])}, w3 = {cvtpk(p1[8], p1[9]), cvtpk(p1[10], p1[11]), cvtpk(p1[12], p1[13]), cvtpk(p1[14], p1[15])};
;         pa0 = *reinterpret_cast<bf16x8*>(&w0); pa1 = *reinterpret_cast<bf16x8*>(&w1); pa2 = *reinterpret_cast<bf16x8*>(&w2); pa3 = *reinterpret_cast<bf16x8*>(&w3); }
;     else { ATT_SOFTMAX(t == 0); }
;     if constexpr (!(ABL & 4)) { ATT_WRITE_K(k2); ATT_WRITE_V(v1); }
;     ATT_SBAR();
; #pragma unroll
;     for (int ks = 0; ks < 4; ++ks) ATT_VPAIR(va, v0, 0, ks);
;     asm volatile("s_waitcnt lgkmcnt(8)" ::: "memory"); ATT_BAR();
;     ATT_XSECTION(true);
;     if constexpr (!(ABL & 4)) { const int tk = (t + 3 < NT) ? t + 3 : NT - 1, tv = (t + 2 < NT) ? t + 2 : NT - 1; ATT_LOAD_K(tk); ATT_LOAD_V(tv); }
;     ATT_BAR();
;     { const int tk_ = k0; k0 = k1; k1 = k2; k2 = tk_; const int tv_ = v0; v0 = v1; v1 = v2; v2 = tv_; }
	s_setprio 2
	s_waitcnt lgkmcnt(7)
	v_mfma_f32_32x32x16_bf16 v[98:113], v[152:155], v[136:139], v[82:97]
	s_waitcnt lgkmcnt(6)
	v_mfma_f32_32x32x16_bf16 v[114:129], v[156:159], v[136:139], v[82:97]
	v_add_u32_e32 v248, s37, v131
	s_waitcnt lgkmcnt(5)
	v_mfma_f32_32x32x16_bf16 v[98:113], v[160:163], v[140:143], v[98:113]
	ds_read_b64_tr_b16 v[198:199], v248
	ds_read_b64_tr_b16 v[200:201], v248 offset:2048
	s_waitcnt lgkmcnt(6)
	v_mfma_f32_32x32x16_bf16 v[114:129], v[176:179], v[140:143], v[114:129]
	ds_read_b64_tr_b16 v[212:213], v248 offset:4096
	ds_read_b64_tr_b16 v[214:215], v248 offset:6144
	s_waitcnt lgkmcnt(7)
	v_mfma_f32_32x32x16_bf16 v[98:113], v[180:183], v[144:147], v[98:113]
	ds_read_b64_tr_b16 v[216:217], v248 offset:8192
	ds_read_b64_tr_b16 v[218:219], v248 offset:10240
	s_waitcnt lgkmcnt(8)
	v_mfma_f32_32x32x16_bf16 v[114:129], v[186:189], v[144:147], v[114:129]
	ds_read_b64_tr_b16 v[220:221], v248 offset:12288
	ds_read_b64_tr_b16 v[222:223], v248 offset:14336
	s_waitcnt lgkmcnt(9)
	v_mfma_f32_32x32x16_bf16 v[98:113], v[190:193], v[148:151], v[98:113]
	s_waitcnt lgkmcnt(8)
	v_mfma_f32_32x32x16_bf16 v[114:129], v[194:197], v[148:151], v[114:129]
	s_waitcnt lgkmcnt(6)
	v_mfma_f32_32x32x16_bf16 v[18:33], v[2:5], v[198:201], v[18:33]
	ds_read_b64_tr_b16 v[236:237], v248 offset:512
	ds_read_b64_tr_b16 v[238:239], v248 offset:2560
	s_waitcnt lgkmcnt(6)
	v_mfma_f32_32x32x16_bf16 v[18:33], v[6:9], v[212:215], v[18:33]
	ds_read_b64_tr_b16 v[198:199], v248 offset:4608
	ds_read_b64_tr_b16 v[200:201], v248 offset:6656
	s_waitcnt lgkmcnt(6)
	v_mfma_f32_32x32x16_bf16 v[18:33], v[10:13], v[216:219], v[18:33]
	ds_read_b64_tr_b16 v[212:213], v248 offset:8704
	ds_read_b64_tr_b16 v[214:215], v248 offset:10752
	s_waitcnt lgkmcnt(6)
	v_mfma_f32_32x32x16_bf16 v[18:33], v[14:17], v[220:223], v[18:33]
	ds_read_b64_tr_b16 v[216:217], v248 offset:12800
	ds_read_b64_tr_b16 v[218:219], v248 offset:14848
	v_max3_f32 v249, v98, v99, v100
	s_waitcnt lgkmcnt(6)
	v_mfma_f32_32x32x16_bf16 v[34:49], v[2:5], v[236:239], v[34:49]
	ds_read_b64_tr_b16 v[220:221], v248 offset:1024
	ds_read_b64_tr_b16 v[222:223], v248 offset:3072
	v_max3_f32 v173, v114, v115, v116
	s_waitcnt lgkmcnt(6)
	v_mfma_f32_32x32x16_bf16 v[34:49], v[6:9], v[198:201], v[34:49]
	ds_read_b64_tr_b16 v[236:237], v248 offset:5120
	ds_read_b64_tr_b16 v[238:239], v248 offset:7168
	v_max3_f32 v249, v249, v101, v102
	s_waitcnt lgkmcnt(6)
	v_mfma_f32_32x32x16_bf16 v[34:49], v[10:13], v[212:215], v[34:49]
	ds_read_b64_tr_b16 v[198:199], v248 offset:9216
	ds_read_b64_tr_b16 v[200:201], v248 offset:11264
	v_max3_f32 v173, v173, v117, v118
	s_waitcnt lgkmcnt(6)
	v_mfma_f32_32x32x16_bf16 v[34:49], v[14:17], v[216:219], v[34:49]
	ds_read_b64_tr_b16 v[212:213], v248 offset:13312
	ds_read_b64_tr_b16 v[214:215], v248 offset:15360
	v_max3_f32 v249, v249, v103, v104
	s_waitcnt lgkmcnt(6)
	v_mfma_f32_32x32x16_bf16 v[50:65], v[2:5], v[220:223], v[50:65]
	ds_read_b64_tr_b16 v[216:217], v248 offset:1536
	ds_read_b64_tr_b16 v[218:219], v248 offset:3584
	v_max3_f32 v173, v173, v119, v120
	s_waitcnt lgkmcnt(6)
	v_mfma_f32_32x32x16_bf16 v[50:65], v[6:9], v[236:239], v[50:65]
	ds_read_b64_tr_b16 v[220:221], v248 offset:5632
	ds_read_b64_tr_b16 v[222:223], v248 offset:7680
	v_max3_f32 v249, v249, v105, v106
	s_waitcnt lgkmcnt(6)
	v_mfma_f32_32x32x16_bf16 v[50:65], v[10:13], v[198:201], v[50:65]
	ds_read_b64_tr_b16 v[236:237], v248 offset:9728
	ds_read_b64_tr_b16 v[238:239], v248 offset:11776
	v_max3_f32 v173, v173, v121, v122
	s_waitcnt lgkmcnt(6)
	v_mfma_f32_32x32x16_bf16 v[50:65], v[14:17], v[212:215], v[50:65]
	ds_read_b64_tr_b16 v[198:199], v248 offset:13824
	ds_read_b64_tr_b16 v[200:201], v248 offset:15872
	v_max3_f32 v249, v249, v107, v108
	s_waitcnt lgkmcnt(6)
	v_mfma_f32_32x32x16_bf16 v[66:81], v[2:5], v[216:219], v[66:81]
	v_max3_f32 v173, v173, v123, v124
	s_min_u32 s14, s97, 0x7c
	s_lshl_b32 s14, s14, 17
	s_add_i32 s14, s14, 0x60000
	buffer_load_dwordx4 v[224:227], v170, s[8:11], s14 offen
	s_waitcnt lgkmcnt(4)
	v_mfma_f32_32x32x16_bf16 v[66:81], v[6:9], v[220:223], v[66:81]
	v_max3_f32 v249, v249, v109, v110
	s_add_i32 s19, s36, 0xffff0000
	s_mov_b32 s14, s10
	s_mov_b32 s15, s11
	buffer_load_dwordx4 v[228:231], v171, s[12:15], s19 offen
	s_waitcnt lgkmcnt(2)
	v_mfma_f32_32x32x16_bf16 v[66:81], v[10:13], v[236:239], v[66:81]
	v_max3_f32 v173, v173, v125, v126
	buffer_load_dwordx4 v[232:235], v171, s[12:15], s36 offen
	s_waitcnt lgkmcnt(0)
	v_mfma_f32_32x32x16_bf16 v[66:81], v[14:17], v[198:201], v[66:81]
	v_max3_f32 v249, v249, v111, v112
	v_mfma_f32_4x4x4_16b_bf16 v[240:243], v[2:3], v[132:133], v[240:243]
	v_max3_f32 v173, v173, v127, v128
	v_mfma_f32_4x4x4_16b_bf16 v[244:247], v[4:5], v[132:133], v[244:247]
	v_mfma_f32_4x4x4_16b_bf16 v[240:243], v[6:7], v[132:133], v[240:243]
	v_max_f32 v249, v249, v113
	v_mfma_f32_4x4x4_16b_bf16 v[244:247], v[8:9], v[132:133], v[244:247]
	v_mfma_f32_4x4x4_16b_bf16 v[240:243], v[10:11], v[132:133], v[240:243]
	v_max_f32 v173, v173, v129
	v_mfma_f32_4x4x4_16b_bf16 v[244:247], v[12:13], v[132:133], v[244:247]
	v_mfma_f32_4x4x4_16b_bf16 v[240:243], v[14:15], v[132:133], v[240:243]
	v_max_f32 v173, v173, v249
	v_mfma_f32_4x4x4_16b_bf16 v[244:247], v[16:17], v[132:133], v[244:247]
	s_setprio 0
	s_barrier
	s_add_i32 s36, s36, 0x20000
	s_add_i32 s97, s97, 1
	s_cmpk_eq_i32 s97, 0x7e
	s_cbranch_scc1 .LBB0_290
	s_mov_b32 s14, s94
	s_mov_b32 s94, s18
	s_mov_b32 s18, s96
	s_mov_b32 s15, s95
	s_mov_b32 s95, s93
	s_mov_b32 s93, s37
	s_branch .LBB0_282

; #define ATT_SBAR() __builtin_amdgcn_sched_barrier(0)
; #define ATT_PK4(P, BASE, OUT) do { u32x4 w = {cvtpk(P[BASE + 0], P[BASE + 1]), cvtpk(P[BASE + 2], P[BASE + 3]), cvtpk(P[BASE + 4], P[BASE + 5]), cvtpk(P[BASE + 6], P[BASE + 7])}; \
;     OUT = *reinterpret_cast<bf16x8*>(&w); } while (0)
; #define ATT_WRITE_K(so) do { *(bf16x8*)(K_lds + (so) + kswz<DQK>(kr, kc * 2)) = sk0; if constexpr (DQK == 128) *(bf16x8*)(K_lds + (so) + kswz<DQK>(32 + kr, kc * 2)) = sk1; } while (0)
; #define ATT_WRITE_V(so) do { *(bf16x8*)(V_lds + (so) + vst0) = sv0; *(bf16x8*)(V_lds + (so) + vst1) = sv1; } while (0)
; #define ATT_BAR() do { ATT_SBAR(); asm volatile("s_barrier" ::: "memory"); ATT_SBAR(); } while (0)
; #define ATT_VPAIR(buf, so, blk, ks) do { if constexpr (!(ABL & 8) && !(ABL & 32)) { buf[2 * (ks)] = vtr(vq0 + (so) + v_rd_off(blk, ks, 0)); buf[2 * (ks) + 1] = vtr(vq0 + (so) + v_rd_off(blk, ks, 1)); } } while (0)
; __device__ __forceinline__ void softmax_exp_pack(f32x16& p0, f32x16& p1, bf16x8& pa0, bf16x8& pa1, bf16x8& pa2, bf16x8& pa3) {
; #pragma unroll
;   for (int r = 0; r < 16; ++r) { p0[r] = __builtin_amdgcn_exp2f(p0[r]); p1[r] = __builtin_amdgcn_exp2f(p1[r]); }
;     ...
;   ATT_PK4(p0, 0, pa0); ATT_PK4(p0, 8, pa1); ATT_PK4(p1, 0, pa2); ATT_PK4(p1, 8, pa3);
;     ...
;     if constexpr (!(ABL & 4)) { ATT_WRITE_K(k2); ATT_WRITE_V(v1); }
;     ATT_SBAR();
; #pragma unroll
;     for (int ks = 0; ks < 4; ++ks) ATT_VPAIR(va, v0, 0, ks);
;     asm volatile("s_waitcnt lgkmcnt(8)" ::: "memory"); ATT_BAR();
.LBB0_298:
	v_exp_f32_e32 v98, v98
	v_exp_f32_e32 v114, v114
	v_exp_f32_e32 v99, v99
	v_exp_f32_e32 v115, v115
	v_exp_f32_e32 v100, v100
	v_exp_f32_e32 v101, v101
	v_exp_f32_e32 v102, v102
	v_exp_f32_e32 v103, v103
	v_exp_f32_e32 v106, v106
	v_exp_f32_e32 v107, v107
	v_exp_f32_e32 v116, v116
	v_exp_f32_e32 v117, v117
	v_exp_f32_e32 v118, v118
	v_exp_f32_e32 v119, v119
	v_exp_f32_e32 v104, v104
	v_exp_f32_e32 v120, v120
	v_exp_f32_e32 v105, v105
	v_exp_f32_e32 v121, v121
	v_exp_f32_e32 v122, v122
	v_exp_f32_e32 v123, v123
	v_exp_f32_e32 v108, v108
	v_exp_f32_e32 v124, v124
	v_exp_f32_e32 v109, v109
	v_exp_f32_e32 v125, v125
	v_exp_f32_e32 v110, v110
	v_exp_f32_e32 v126, v126
	v_exp_f32_e32 v111, v111
	v_exp_f32_e32 v127, v127
	v_exp_f32_e32 v112, v112
	v_exp_f32_e32 v128, v128
	v_exp_f32_e32 v113, v113
	v_exp_f32_e32 v129, v129
	v_cvt_pk_bf16_f32 v18, v98, v99
	v_cvt_pk_bf16_f32 v19, v100, v101
	v_cvt_pk_bf16_f32 v20, v102, v103
	v_cvt_pk_bf16_f32 v22, v106, v107
	v_cvt_pk_bf16_f32 v26, v114, v115
	v_cvt_pk_bf16_f32 v21, v104, v105
	v_cvt_pk_bf16_f32 v23, v108, v109
	v_cvt_pk_bf16_f32 v24, v110, v111
	v_cvt_pk_bf16_f32 v25, v112, v113
	v_cvt_pk_bf16_f32 v27, v116, v117
	v_cvt_pk_bf16_f32 v28, v118, v119
	v_cvt_pk_bf16_f32 v29, v120, v121
	v_cvt_pk_bf16_f32 v30, v122, v123
	v_cvt_pk_bf16_f32 v31, v124, v125
	v_cvt_pk_bf16_f32 v32, v126, v127
	v_cvt_pk_bf16_f32 v33, v128, v129
	s_waitcnt vmcnt(0)
	v_add_u32_e32 v114, s49, v170
	ds_write_b128 v114, v[224:227] offset:49152
	v_add_u32_e32 v114, s50, v168
	ds_write_b128 v114, v[228:231]
	v_add_u32_e32 v114, s50, v169
	ds_write_b128 v114, v[232:235]
	v_add_u32_e32 v249, s18, v173
	ds_read_b128 v[152:155], v249 offset:49152
	ds_read_b128 v[156:159], v249 offset:53760
	ds_read_b128 v[160:163], v249 offset:49184
	ds_read_b128 v[176:179], v249 offset:53792
	ds_read_b128 v[180:183], v249 offset:49216
	ds_read_b128 v[186:189], v249 offset:53824
	ds_read_b128 v[190:193], v249 offset:49248
	ds_read_b128 v[194:197], v249 offset:53856
	s_waitcnt lgkmcnt(8)
	s_barrier
; #define ATT_SBAR() __builtin_amdgcn_sched_barrier(0)
; __device__ __forceinline__ float softmax_rowmax(const f32x16& p0, const f32x16& p1) {
;   const float m0 = p1[0] + 0.0f; float a, b;
;   asm("v_max3_f32 %0, %1, %2, %3\n\tv_max3_f32 %0, %0, %4, %5\n\tv_max3_f32 %0, %0, %6, %7\n\tv_max3_f32 %0, %0, %8, %9\n\t"
;       "v_max3_f32 %0, %0, %10, %11\n\tv_max3_f32 %0, %0, %12, %13\n\tv_max3_f32 %0, %0, %14, %15\n\tv_max3_f32 %0, %0, %16, %17"
;       : "=&v"(a) : "v"(m0), "v"(p0[0]), "v"(p0[1]), "v"(p0[2]), "v"(p0[3]), "v"(p0[4]), "v"(p0[5]), "v"(p0[6]), "v"(p0[7]), "v"(p0[8]), "v"(p0[9]), "v"(p0[10]), "v"(p0[11]), "v"(p0[12]), "v"(p0[13]), "v"(p0[14]), "v"(p0[15]));
;   asm("v_max3_f32 %0, %1, %2, %3\n\tv_max3_f32 %0, %0, %4, %5\n\tv_max3_f32 %0, %0, %6, %7\n\tv_max3_f32 %0, %0, %8, %9\n\t"
;       "v_max3_f32 %0, %0, %10, %11\n\tv_max3_f32 %0, %0, %12, %13\n\tv_max3_f32 %0, %0, %14, %15\n\tv_max_f32 %0, %0, %16"
;       : "=&v"(b) : "v"(a), "v"(p1[1]), "v"(p1[2]), "v"(p1[3]), "v"(p1[4]), "v"(p1[5]), "v"(p1[6]), "v"(p1[7]), "v"(p1[8]), "v"(p1[9]), "v"(p1[10]), "v"(p1[11]), "v"(p1[12]), "v"(p1[13]), "v"(p1[14]), "v"(p1[15]));
;   return b;
;     ...
;   for (int t = 0; t + 1 < NT; ++t) {
;     if constexpr (ABL & 1) { u32x4 w0 = {cvtpk(p0[0], p0[1]), cvtpk(p0[2], p0[3]), cvtpk(p0[4], p0[5]), cvtpk(p0[6], p0[7])}, w1 = {cvtpk(p0[8], p0[9]), cvtpk(p0[10], p0[11]), cvtpk(p0[12], p0[13]), cvtpk(p0[14], p0[15])};
;         u32x4 w2 = {cvtpk(p1[0], p1[1]), cvtpk(p1[2], p1[3]), cvtpk(p1[4], p1[5]), cvtpk(p1[6], p1[7])}, w3 = {cvtpk(p1[8], p1[9]), cvtpk(p1[10], p1[11]), cvtpk(p1[12], p1[13]), cvtpk(p1[14], p1[15])};
;         pa0 = *reinterpret_cast<bf16x8*>(&w0); pa1 = *reinterpret_cast<bf16x8*>(&w1); pa2 = *reinterpret_cast<bf16x8*>(&w2); pa3 = *reinterpret_cast<bf16x8*>(&w3); }
;     else { ATT_SOFTMAX(t == 0); }
;     if constexpr (!(ABL & 4)) { ATT_WRITE_K(k2); ATT_WRITE_V(v1); }
;     ATT_SBAR();
; #pragma unroll
;     for (int ks = 0; ks < 4; ++ks) ATT_VPAIR(va, v0, 0, ks);
;     asm volatile("s_waitcnt lgkmcnt(8)" ::: "memory"); ATT_BAR();
;     ATT_XSECTION(true);
;     if constexpr (!(ABL & 4)) { const int tk = (t + 3 < NT) ? t + 3 : NT - 1, tv = (t + 2 < NT) ? t + 2 : NT - 1; ATT_LOAD_K(tk); ATT_LOAD_V(tv); }
;     ATT_BAR();
;     { const int tk_ = k0; k0 = k1; k1 = k2; k2 = tk_; const int tv_ = v0; v0 = v1; v1 = v2; v2 = tv_; }
	s_setprio 2
	s_waitcnt lgkmcnt(7)
	v_mfma_f32_32x32x16_bf16 v[98:113], v[152:155], v[136:139], v[82:97]
	s_waitcnt lgkmcnt(6)
	v_mfma_f32_32x32x16_bf16 v[114:129], v[156:159], v[136:139], v[82:97]
	v_add_u32_e32 v248, s37, v131
	s_waitcnt lgkmcnt(5)
	v_mfma_f32_32x32x16_bf16 v[98:113], v[160:163], v[140:143], v[98:113]
	ds_read_b64_tr_b16 v[198:199], v248
	ds_read_b64_tr_b16 v[200:201], v248 offset:2048
	s_waitcnt lgkmcnt(6)
	v_mfma_f32_32x32x16_bf16 v[114:129], v[176:179], v[140:143], v[114:129]
	ds_read_b64_tr_b16 v[212:213], v248 offset:4096
	ds_read_b64_tr_b16 v[214:215], v248 offset:6144
	s_waitcnt lgkmcnt(7)
	v_mfma_f32_32x32x16_bf16 v[98:113], v[180:183], v[144:147], v[98:113]
	ds_read_b64_tr_b16 v[216:217], v248 offset:8192
	ds_read_b64_tr_b16 v[218:219], v248 offset:10240
	s_waitcnt lgkmcnt(8)
	v_mfma_f32_32x32x16_bf16 v[114:129], v[186:189], v[144:147], v[114:129]
	ds_read_b64_tr_b16 v[220:221], v248 offset:12288
	ds_read_b64_tr_b16 v[222:223], v248 offset:14336
	s_waitcnt lgkmcnt(9)
	v_mfma_f32_32x32x16_bf16 v[98:113], v[190:193], v[148:151], v[98:113]
	s_waitcnt lgkmcnt(8)
	v_mfma_f32_32x32x16_bf16 v[114:129], v[194:197], v[148:151], v[114:129]
	s_waitcnt lgkmcnt(6)
	v_mfma_f32_32x32x16_bf16 v[66:81], v[18:21], v[198:201], v[66:81]
	ds_read_b64_tr_b16 v[236:237], v248 offset:512
	ds_read_b64_tr_b16 v[238:239], v248 offset:2560
	s_waitcnt lgkmcnt(6)
	v_mfma_f32_32x32x16_bf16 v[66:81], v[22:25], v[212:215], v[66:81]
	ds_read_b64_tr_b16 v[198:199], v248 offset:4608
	ds_read_b64_tr_b16 v[200:201], v248 offset:6656
	s_waitcnt lgkmcnt(6)
	v_mfma_f32_32x32x16_bf16 v[66:81], v[26:29], v[216:219], v[66:81]
	ds_read_b64_tr_b16 v[212:213], v248 offset:8704
	ds_read_b64_tr_b16 v[214:215], v248 offset:10752
	s_waitcnt lgkmcnt(6)
	v_mfma_f32_32x32x16_bf16 v[66:81], v[30:33], v[220:223], v[66:81]
	ds_read_b64_tr_b16 v[216:217], v248 offset:12800
	ds_read_b64_tr_b16 v[218:219], v248 offset:14848
	v_max3_f32 v249, v98, v99, v100
	s_waitcnt lgkmcnt(6)
	v_mfma_f32_32x32x16_bf16 v[50:65], v[18:21], v[236:239], v[50:65]
	ds_read_b64_tr_b16 v[220:221], v248 offset:1024
	ds_read_b64_tr_b16 v[222:223], v248 offset:3072
	v_max3_f32 v174, v114, v115, v116
	s_waitcnt lgkmcnt(6)
	v_mfma_f32_32x32x16_bf16 v[50:65], v[22:25], v[198:201], v[50:65]
	ds_read_b64_tr_b16 v[236:237], v248 offset:5120
	ds_read_b64_tr_b16 v[238:239], v248 offset:7168
	v_max3_f32 v249, v249, v101, v102
	s_waitcnt lgkmcnt(6)
	v_mfma_f32_32x32x16_bf16 v[50:65], v[26:29], v[212:215], v[50:65]
	ds_read_b64_tr_b16 v[198:199], v248 offset:9216
	ds_read_b64_tr_b16 v[200:201], v248 offset:11264
	v_max3_f32 v174, v174, v117, v118
	s_waitcnt lgkmcnt(6)
	v_mfma_f32_32x32x16_bf16 v[50:65], v[30:33], v[216:219], v[50:65]
	ds_read_b64_tr_b16 v[212:213], v248 offset:13312
	ds_read_b64_tr_b16 v[214:215], v248 offset:15360
	v_max3_f32 v249, v249, v103, v104
	s_waitcnt lgkmcnt(6)
	v_mfma_f32_32x32x16_bf16 v[34:49], v[18:21], v[220:223], v[34:49]
	ds_read_b64_tr_b16 v[216:217], v248 offset:1536
	ds_read_b64_tr_b16 v[218:219], v248 offset:3584
	v_max3_f32 v174, v174, v119, v120
	s_waitcnt lgkmcnt(6)
	v_mfma_f32_32x32x16_bf16 v[34:49], v[22:25], v[236:239], v[34:49]
	ds_read_b64_tr_b16 v[220:221], v248 offset:5632
	ds_read_b64_tr_b16 v[222:223], v248 offset:7680
	v_max3_f32 v249, v249, v105, v106
	s_waitcnt lgkmcnt(6)
	v_mfma_f32_32x32x16_bf16 v[34:49], v[26:29], v[198:201], v[34:49]
	ds_read_b64_tr_b16 v[236:237], v248 offset:9728
	ds_read_b64_tr_b16 v[238:239], v248 offset:11776
	v_max3_f32 v174, v174, v121, v122
	s_waitcnt lgkmcnt(6)
	v_mfma_f32_32x32x16_bf16 v[34:49], v[30:33], v[212:215], v[34:49]
	ds_read_b64_tr_b16 v[198:199], v248 offset:13824
	ds_read_b64_tr_b16 v[200:201], v248 offset:15872
	v_max3_f32 v249, v249, v107, v108
	s_waitcnt lgkmcnt(6)
	v_mfma_f32_32x32x16_bf16 v[2:17], v[18:21], v[216:219], v[2:17]
	v_max3_f32 v174, v174, v123, v124
	s_min_u32 s14, s90, 0x7c
	s_lshl_b32 s14, s14, 17
	s_add_i32 s19, s14, 0x60000
	s_add_i32 s92, s36, 0xffff0000
	s_mov_b32 s14, s10
	s_mov_b32 s15, s11
	buffer_load_dwordx4 v[224:227], v171, s[8:11], s19 offen
	s_waitcnt lgkmcnt(4)
	v_mfma_f32_32x32x16_bf16 v[2:17], v[22:25], v[220:223], v[2:17]
	v_max3_f32 v249, v249, v109, v110
	buffer_load_dwordx4 v[228:231], v172, s[12:15], s92 offen
	s_waitcnt lgkmcnt(2)
	v_mfma_f32_32x32x16_bf16 v[2:17], v[26:29], v[236:239], v[2:17]
	v_max3_f32 v174, v174, v125, v126
	buffer_load_dwordx4 v[232:235], v172, s[12:15], s36 offen
	s_waitcnt lgkmcnt(0)
	v_mfma_f32_32x32x16_bf16 v[2:17], v[30:33], v[198:201], v[2:17]
	v_max3_f32 v249, v249, v111, v112
	v_mfma_f32_4x4x4_16b_bf16 v[240:243], v[18:19], v[132:133], v[240:243]
	v_max3_f32 v174, v174, v127, v128
	v_mfma_f32_4x4x4_16b_bf16 v[244:247], v[20:21], v[132:133], v[244:247]
	v_mfma_f32_4x4x4_16b_bf16 v[240:243], v[22:23], v[132:133], v[240:243]
	v_max_f32 v249, v249, v113
	v_mfma_f32_4x4x4_16b_bf16 v[244:247], v[24:25], v[132:133], v[244:247]
	v_mfma_f32_4x4x4_16b_bf16 v[240:243], v[26:27], v[132:133], v[240:243]
	v_max_f32 v174, v174, v129
	v_mfma_f32_4x4x4_16b_bf16 v[244:247], v[28:29], v[132:133], v[244:247]
	v_mfma_f32_4x4x4_16b_bf16 v[240:243], v[30:31], v[132:133], v[240:243]
	v_max_f32 v174, v174, v249
	v_mfma_f32_4x4x4_16b_bf16 v[244:247], v[32:33], v[132:133], v[244:247]
	s_setprio 0
	s_barrier
	s_add_i32 s36, s36, 0x20000
	s_add_i32 s90, s90, 1
	s_cmpk_eq_i32 s90, 0x7e
	s_cbranch_scc1 .LBB0_305
	s_mov_b32 s14, s49
	s_mov_b32 s49, s51
	s_mov_b32 s51, s18
	s_mov_b32 s15, s50
	s_mov_b32 s50, s48
	s_mov_b32 s48, s37
	s_branch .LBB0_297
